# PEER gather u-pass: per-token reduce-scatter over 8 lanes via DPP moves (row_shl/shr:4 + quad_perm) instead of three ds_bpermute round trips; on top of v062
# baseline (speedup 1.0000x reference)
.LBB0_746:
	ds_read_b128 v[2:5], v123
	ds_read_b128 v[82:85], v123 offset:128
	v_mov_b32_e32 v94, 0
	v_mov_b32_e32 v96, 0
	v_mov_b32_e32 v98, 0
	s_waitcnt lgkmcnt(0)
	v_and_b32_e32 v6, 0xffff, v2
	v_lshrrev_b32_e32 v2, 16, v2
	v_mad_u32_u24 v6, v6, s30, v110
	v_mad_u32_u24 v2, v2, s30, v110
	global_load_dwordx2 v[10:11], v6, s[26:27] offset:16
	s_nop 0
	global_load_dwordx4 v[6:9], v6, s[26:27]
	s_nop 0
	global_load_dwordx2 v[16:17], v2, s[26:27] offset:16
	global_load_dwordx4 v[12:15], v2, s[26:27]
	v_and_b32_e32 v2, 0xffff, v3
	v_mad_u32_u24 v2, v2, s30, v110
	global_load_dwordx2 v[130:131], v2, s[26:27] offset:16
	global_load_dwordx4 v[126:129], v2, s[26:27]
	v_lshrrev_b32_e32 v2, 16, v3
	v_mad_u32_u24 v2, v2, s30, v110
	global_load_dwordx2 v[136:137], v2, s[26:27] offset:16
	global_load_dwordx4 v[132:135], v2, s[26:27]
	v_and_b32_e32 v2, 0xffff, v4
	v_mad_u32_u24 v2, v2, s30, v110
	global_load_dwordx2 v[142:143], v2, s[26:27] offset:16
	global_load_dwordx4 v[138:141], v2, s[26:27]
	v_lshrrev_b32_e32 v3, 16, v4
	v_and_b32_e32 v2, 0xffff, v5
	v_lshrrev_b32_e32 v4, 16, v5
	v_mad_u32_u24 v3, v3, s30, v110
	v_mad_u32_u24 v2, v2, s30, v110
	v_mad_u32_u24 v4, v4, s30, v110
	global_load_dwordx2 v[148:149], v3, s[26:27] offset:16
	global_load_dwordx4 v[144:147], v3, s[26:27]
	global_load_dwordx2 v[154:155], v2, s[26:27] offset:16
	global_load_dwordx4 v[150:153], v2, s[26:27]
	global_load_dwordx2 v[160:161], v4, s[26:27] offset:16
	global_load_dwordx4 v[156:159], v4, s[26:27]
	v_mov_b32_e32 v102, 0
	v_mov_b32_e32 v104, 0
	v_mov_b32_e32 v100, 0
	v_mov_b32_e32 v106, 0
	v_mov_b32_e32 v108, 0
	v_mov_b32_e32 v107, 0
	v_mov_b32_e32 v109, 0
	v_mov_b32_e32 v103, 0
	v_mov_b32_e32 v105, 0
	v_mov_b32_e32 v99, 0
	v_mov_b32_e32 v101, 0
	v_mov_b32_e32 v95, 0
	v_mov_b32_e32 v97, 0
	s_and_b64 vcc, exec, s[12:13]
	s_waitcnt vmcnt(14)
	v_cvt_scalef32_pk32_bf16_fp6 v[50:65], v[6:11], 1.0
	v_dot2c_f32_bf16_e32 v106, v50, v78
	s_waitcnt vmcnt(12)
	v_cvt_scalef32_pk32_bf16_fp6 v[34:49], v[12:17], 1.0
	v_dot2c_f32_bf16_e32 v102, v34, v78
	v_dot2c_f32_bf16_e32 v104, v35, v79
	s_waitcnt vmcnt(10)
	v_cvt_scalef32_pk32_bf16_fp6 v[18:33], v[126:131], 1.0
	v_dot2c_f32_bf16_e32 v98, v18, v78
	v_dot2c_f32_bf16_e32 v98, v20, v80
	s_waitcnt vmcnt(8)
	v_cvt_scalef32_pk32_bf16_fp6 v[2:17], v[132:137], 1.0
	v_dot2c_f32_bf16_e32 v94, v2, v78
	v_dot2c_f32_bf16_e32 v96, v3, v79
	v_dot2c_f32_bf16_e32 v94, v4, v80
	v_dot2c_f32_bf16_e32 v96, v5, v81
	v_dot2c_f32_bf16_e32 v94, v6, v74
	v_dot2c_f32_bf16_e32 v96, v7, v75
	v_dot2c_f32_bf16_e32 v94, v8, v76
	v_dot2c_f32_bf16_e32 v96, v9, v77
	v_dot2c_f32_bf16_e32 v94, v10, v70
	v_dot2c_f32_bf16_e32 v96, v11, v71
	v_dot2c_f32_bf16_e32 v94, v12, v72
	v_dot2c_f32_bf16_e32 v96, v13, v73
	v_dot2c_f32_bf16_e32 v94, v14, v66
	v_dot2c_f32_bf16_e32 v96, v15, v67
	v_dot2c_f32_bf16_e32 v94, v16, v68
	v_dot2c_f32_bf16_e32 v96, v17, v69
	s_waitcnt vmcnt(6)
	v_cvt_scalef32_pk32_bf16_fp6 v[2:17], v[138:143], 1.0
	v_mov_b32_e32 v18, 0
	v_mov_b32_e32 v20, 0
	v_dot2c_f32_bf16_e32 v18, v2, v78
	v_dot2c_f32_bf16_e32 v20, v3, v79
	v_dot2c_f32_bf16_e32 v18, v4, v80
	v_dot2c_f32_bf16_e32 v20, v5, v81
	v_dot2c_f32_bf16_e32 v18, v6, v74
	v_dot2c_f32_bf16_e32 v20, v7, v75
	v_dot2c_f32_bf16_e32 v18, v8, v76
	v_dot2c_f32_bf16_e32 v20, v9, v77
	v_dot2c_f32_bf16_e32 v18, v10, v70
	v_dot2c_f32_bf16_e32 v20, v11, v71
	v_dot2c_f32_bf16_e32 v18, v12, v72
	v_dot2c_f32_bf16_e32 v20, v13, v73
	v_dot2c_f32_bf16_e32 v18, v14, v66
	v_dot2c_f32_bf16_e32 v20, v15, v67
	v_dot2c_f32_bf16_e32 v98, v22, v74
	v_dot2c_f32_bf16_e32 v18, v16, v68
	v_dot2c_f32_bf16_e32 v20, v17, v69
	s_waitcnt vmcnt(4)
	v_cvt_scalef32_pk32_bf16_fp6 v[2:17], v[144:149], 1.0
	v_mov_b32_e32 v22, 0
	v_dot2c_f32_bf16_e32 v22, v2, v78
	v_and_b32_e32 v2, 0xffff, v82
	v_dot2c_f32_bf16_e32 v102, v36, v80
	v_dot2c_f32_bf16_e32 v104, v37, v81
	v_mad_u32_u24 v2, v2, s30, v110
	v_dot2c_f32_bf16_e32 v102, v38, v74
	v_dot2c_f32_bf16_e32 v104, v39, v75
	global_load_dwordx2 v[38:39], v2, s[26:27] offset:16
	global_load_dwordx4 v[34:37], v2, s[26:27]
	v_dot2c_f32_bf16_e32 v98, v24, v76
	v_mov_b32_e32 v24, 0
	v_dot2c_f32_bf16_e32 v100, v19, v79
	v_dot2c_f32_bf16_e32 v102, v40, v76
	v_dot2c_f32_bf16_e32 v104, v41, v77
	v_dot2c_f32_bf16_e32 v24, v3, v79
	v_lshrrev_b32_e32 v19, 16, v82
	v_dot2c_f32_bf16_e32 v102, v42, v70
	v_dot2c_f32_bf16_e32 v104, v43, v71
	v_dot2c_f32_bf16_e32 v22, v4, v80
	v_dot2c_f32_bf16_e32 v24, v5, v81
	v_mad_u32_u24 v19, v19, s30, v110
	v_dot2c_f32_bf16_e32 v102, v44, v72
	v_dot2c_f32_bf16_e32 v104, v45, v73
	v_dot2c_f32_bf16_e32 v22, v6, v74
	v_dot2c_f32_bf16_e32 v24, v7, v75
	global_load_dwordx2 v[44:45], v19, s[26:27] offset:16
	global_load_dwordx4 v[40:43], v19, s[26:27]
	v_dot2c_f32_bf16_e32 v22, v8, v76
	v_dot2c_f32_bf16_e32 v24, v9, v77
	v_dot2c_f32_bf16_e32 v22, v10, v70
	v_dot2c_f32_bf16_e32 v24, v11, v71
	v_dot2c_f32_bf16_e32 v22, v12, v72
	v_dot2c_f32_bf16_e32 v24, v13, v73
	v_dot2c_f32_bf16_e32 v98, v26, v70
	v_dot2c_f32_bf16_e32 v22, v14, v66
	v_dot2c_f32_bf16_e32 v24, v15, v67
	v_dot2c_f32_bf16_e32 v98, v28, v72
	v_dot2c_f32_bf16_e32 v22, v16, v68
	v_dot2c_f32_bf16_e32 v24, v17, v69
	s_waitcnt vmcnt(6)
	v_cvt_scalef32_pk32_bf16_fp6 v[2:17], v[150:155], 1.0
	v_mov_b32_e32 v26, 0
	v_mov_b32_e32 v28, 0
	v_dot2c_f32_bf16_e32 v26, v2, v78
	v_dot2c_f32_bf16_e32 v28, v3, v79
	v_and_b32_e32 v2, 0xffff, v83
	v_dot2c_f32_bf16_e32 v102, v46, v66
	v_dot2c_f32_bf16_e32 v104, v47, v67
	v_dot2c_f32_bf16_e32 v26, v4, v80
	v_dot2c_f32_bf16_e32 v28, v5, v81
	v_mad_u32_u24 v2, v2, s30, v110
	v_dot2c_f32_bf16_e32 v108, v51, v79
	v_dot2c_f32_bf16_e32 v102, v48, v68
	v_dot2c_f32_bf16_e32 v104, v49, v69
	v_dot2c_f32_bf16_e32 v26, v6, v74
	v_dot2c_f32_bf16_e32 v28, v7, v75
	global_load_dwordx2 v[50:51], v2, s[26:27] offset:16
	global_load_dwordx4 v[46:49], v2, s[26:27]
	v_dot2c_f32_bf16_e32 v26, v8, v76
	v_dot2c_f32_bf16_e32 v28, v9, v77
	v_dot2c_f32_bf16_e32 v26, v10, v70
	v_dot2c_f32_bf16_e32 v28, v11, v71
	v_dot2c_f32_bf16_e32 v26, v12, v72
	v_dot2c_f32_bf16_e32 v28, v13, v73
	v_dot2c_f32_bf16_e32 v26, v14, v66
	v_dot2c_f32_bf16_e32 v28, v15, v67
	v_dot2c_f32_bf16_e32 v98, v30, v66
	v_dot2c_f32_bf16_e32 v26, v16, v68
	v_dot2c_f32_bf16_e32 v28, v17, v69
	s_waitcnt vmcnt(6)
	v_cvt_scalef32_pk32_bf16_fp6 v[2:17], v[156:161], 1.0
	v_mov_b32_e32 v30, 0
	v_dot2c_f32_bf16_e32 v106, v52, v80
	v_dot2c_f32_bf16_e32 v108, v53, v81
	v_dot2c_f32_bf16_e32 v30, v2, v78
	v_lshrrev_b32_e32 v2, 16, v83
	v_dot2c_f32_bf16_e32 v106, v54, v74
	v_dot2c_f32_bf16_e32 v108, v55, v75
	v_mad_u32_u24 v2, v2, s30, v110
	v_dot2c_f32_bf16_e32 v106, v56, v76
	v_dot2c_f32_bf16_e32 v108, v57, v77
	global_load_dwordx2 v[56:57], v2, s[26:27] offset:16
	global_load_dwordx4 v[52:55], v2, s[26:27]
	v_dot2c_f32_bf16_e32 v106, v58, v70
	v_dot2c_f32_bf16_e32 v108, v59, v71
	v_and_b32_e32 v2, 0xffff, v84
	v_dot2c_f32_bf16_e32 v106, v60, v72
	v_dot2c_f32_bf16_e32 v108, v61, v73
	v_mad_u32_u24 v2, v2, s30, v110
	v_dot2c_f32_bf16_e32 v106, v62, v66
	v_dot2c_f32_bf16_e32 v108, v63, v67
	global_load_dwordx2 v[62:63], v2, s[26:27] offset:16
	global_load_dwordx4 v[58:61], v2, s[26:27]
	v_lshrrev_b32_e32 v2, 16, v84
	v_mad_u32_u24 v2, v2, s30, v110
	global_load_dwordx2 v[130:131], v2, s[26:27] offset:16
	global_load_dwordx4 v[126:129], v2, s[26:27]
	v_and_b32_e32 v2, 0xffff, v85
	v_mad_u32_u24 v2, v2, s30, v110
	global_load_dwordx2 v[136:137], v2, s[26:27] offset:16
	global_load_dwordx4 v[132:135], v2, s[26:27]
	v_lshrrev_b32_e32 v2, 16, v85
	v_mad_u32_u24 v2, v2, s30, v110
	global_load_dwordx2 v[142:143], v2, s[26:27] offset:16
	global_load_dwordx4 v[138:141], v2, s[26:27]
	v_dot2c_f32_bf16_e32 v98, v32, v68
	v_mov_b32_e32 v32, 0
	v_dot2c_f32_bf16_e32 v32, v3, v79
	v_dot2c_f32_bf16_e32 v30, v4, v80
	v_dot2c_f32_bf16_e32 v32, v5, v81
	v_dot2c_f32_bf16_e32 v30, v6, v74
	v_dot2c_f32_bf16_e32 v32, v7, v75
	v_dot2c_f32_bf16_e32 v30, v8, v76
	v_dot2c_f32_bf16_e32 v32, v9, v77
	v_dot2c_f32_bf16_e32 v30, v10, v70
	v_dot2c_f32_bf16_e32 v32, v11, v71
	v_dot2c_f32_bf16_e32 v30, v12, v72
	v_dot2c_f32_bf16_e32 v32, v13, v73
	v_dot2c_f32_bf16_e32 v30, v14, v66
	v_dot2c_f32_bf16_e32 v32, v15, v67
	v_dot2c_f32_bf16_e32 v30, v16, v68
	v_dot2c_f32_bf16_e32 v32, v17, v69
	s_waitcnt vmcnt(14)
	v_cvt_scalef32_pk32_bf16_fp6 v[2:17], v[34:39], 1.0
	v_dot2c_f32_bf16_e32 v107, v2, v78
	v_dot2c_f32_bf16_e32 v109, v3, v79
	v_dot2c_f32_bf16_e32 v107, v4, v80
	v_dot2c_f32_bf16_e32 v109, v5, v81
	v_dot2c_f32_bf16_e32 v107, v6, v74
	v_dot2c_f32_bf16_e32 v109, v7, v75
	v_dot2c_f32_bf16_e32 v107, v8, v76
	v_dot2c_f32_bf16_e32 v109, v9, v77
	v_dot2c_f32_bf16_e32 v107, v10, v70
	v_dot2c_f32_bf16_e32 v109, v11, v71
	v_dot2c_f32_bf16_e32 v107, v12, v72
	v_dot2c_f32_bf16_e32 v109, v13, v73
	v_dot2c_f32_bf16_e32 v107, v14, v66
	v_dot2c_f32_bf16_e32 v109, v15, v67
	v_dot2c_f32_bf16_e32 v107, v16, v68
	v_dot2c_f32_bf16_e32 v109, v17, v69
	s_waitcnt vmcnt(12)
	v_cvt_scalef32_pk32_bf16_fp6 v[2:17], v[40:45], 1.0
	v_dot2c_f32_bf16_e32 v103, v2, v78
	v_dot2c_f32_bf16_e32 v105, v3, v79
	v_dot2c_f32_bf16_e32 v103, v4, v80
	v_dot2c_f32_bf16_e32 v105, v5, v81
	v_dot2c_f32_bf16_e32 v103, v6, v74
	v_dot2c_f32_bf16_e32 v105, v7, v75
	v_dot2c_f32_bf16_e32 v103, v8, v76
	v_dot2c_f32_bf16_e32 v105, v9, v77
	v_dot2c_f32_bf16_e32 v103, v10, v70
	v_dot2c_f32_bf16_e32 v105, v11, v71
	v_dot2c_f32_bf16_e32 v103, v12, v72
	v_dot2c_f32_bf16_e32 v105, v13, v73
	v_dot2c_f32_bf16_e32 v103, v14, v66
	v_dot2c_f32_bf16_e32 v105, v15, v67
	v_dot2c_f32_bf16_e32 v103, v16, v68
	v_dot2c_f32_bf16_e32 v105, v17, v69
	s_waitcnt vmcnt(10)
	v_cvt_scalef32_pk32_bf16_fp6 v[2:17], v[46:51], 1.0
	v_dot2c_f32_bf16_e32 v99, v2, v78
	v_dot2c_f32_bf16_e32 v101, v3, v79
	v_dot2c_f32_bf16_e32 v99, v4, v80
	v_dot2c_f32_bf16_e32 v101, v5, v81
	v_dot2c_f32_bf16_e32 v99, v6, v74
	v_dot2c_f32_bf16_e32 v101, v7, v75
	v_dot2c_f32_bf16_e32 v99, v8, v76
	v_dot2c_f32_bf16_e32 v101, v9, v77
	v_dot2c_f32_bf16_e32 v99, v10, v70
	v_dot2c_f32_bf16_e32 v101, v11, v71
	v_dot2c_f32_bf16_e32 v99, v12, v72
	v_dot2c_f32_bf16_e32 v101, v13, v73
	v_dot2c_f32_bf16_e32 v99, v14, v66
	v_dot2c_f32_bf16_e32 v101, v15, v67
	v_dot2c_f32_bf16_e32 v99, v16, v68
	v_dot2c_f32_bf16_e32 v101, v17, v69
	s_waitcnt vmcnt(8)
	v_cvt_scalef32_pk32_bf16_fp6 v[2:17], v[52:57], 1.0
	v_dot2c_f32_bf16_e32 v95, v2, v78
	v_dot2c_f32_bf16_e32 v97, v3, v79
	v_dot2c_f32_bf16_e32 v95, v4, v80
	v_dot2c_f32_bf16_e32 v97, v5, v81
	v_dot2c_f32_bf16_e32 v95, v6, v74
	v_dot2c_f32_bf16_e32 v97, v7, v75
	v_dot2c_f32_bf16_e32 v95, v8, v76
	v_dot2c_f32_bf16_e32 v97, v9, v77
	v_dot2c_f32_bf16_e32 v95, v10, v70
	v_dot2c_f32_bf16_e32 v97, v11, v71
	v_dot2c_f32_bf16_e32 v95, v12, v72
	v_dot2c_f32_bf16_e32 v97, v13, v73
	v_dot2c_f32_bf16_e32 v95, v14, v66
	v_dot2c_f32_bf16_e32 v97, v15, v67
	v_dot2c_f32_bf16_e32 v100, v21, v81
	v_dot2c_f32_bf16_e32 v95, v16, v68
	v_dot2c_f32_bf16_e32 v97, v17, v69
	s_waitcnt vmcnt(6)
	v_cvt_scalef32_pk32_bf16_fp6 v[2:17], v[58:63], 1.0
	v_mov_b32_e32 v19, 0
	v_mov_b32_e32 v21, 0
	v_dot2c_f32_bf16_e32 v19, v2, v78
	v_dot2c_f32_bf16_e32 v21, v3, v79
	v_dot2c_f32_bf16_e32 v19, v4, v80
	v_dot2c_f32_bf16_e32 v21, v5, v81
	v_dot2c_f32_bf16_e32 v19, v6, v74
	v_dot2c_f32_bf16_e32 v21, v7, v75
	v_dot2c_f32_bf16_e32 v19, v8, v76
	v_dot2c_f32_bf16_e32 v21, v9, v77
	v_dot2c_f32_bf16_e32 v19, v10, v70
	v_dot2c_f32_bf16_e32 v21, v11, v71
	v_dot2c_f32_bf16_e32 v19, v12, v72
	v_dot2c_f32_bf16_e32 v21, v13, v73
	v_dot2c_f32_bf16_e32 v100, v23, v75
	v_dot2c_f32_bf16_e32 v19, v14, v66
	v_dot2c_f32_bf16_e32 v21, v15, v67
	v_dot2c_f32_bf16_e32 v100, v25, v77
	v_dot2c_f32_bf16_e32 v19, v16, v68
	v_dot2c_f32_bf16_e32 v21, v17, v69
	s_waitcnt vmcnt(4)
	v_cvt_scalef32_pk32_bf16_fp6 v[2:17], v[126:131], 1.0
	v_mov_b32_e32 v23, 0
	v_mov_b32_e32 v25, 0
	v_dot2c_f32_bf16_e32 v23, v2, v78
	v_dot2c_f32_bf16_e32 v25, v3, v79
	v_dot2c_f32_bf16_e32 v23, v4, v80
	v_dot2c_f32_bf16_e32 v25, v5, v81
	v_dot2c_f32_bf16_e32 v23, v6, v74
	v_dot2c_f32_bf16_e32 v25, v7, v75
	v_dot2c_f32_bf16_e32 v23, v8, v76
	v_dot2c_f32_bf16_e32 v25, v9, v77
	v_dot2c_f32_bf16_e32 v23, v10, v70
	v_dot2c_f32_bf16_e32 v25, v11, v71
	v_dot2c_f32_bf16_e32 v23, v12, v72
	v_dot2c_f32_bf16_e32 v25, v13, v73
	v_dot2c_f32_bf16_e32 v100, v27, v71
	v_dot2c_f32_bf16_e32 v23, v14, v66
	v_dot2c_f32_bf16_e32 v25, v15, v67
	v_dot2c_f32_bf16_e32 v100, v29, v73
	v_dot2c_f32_bf16_e32 v23, v16, v68
	v_dot2c_f32_bf16_e32 v25, v17, v69
	s_waitcnt vmcnt(2)
	v_cvt_scalef32_pk32_bf16_fp6 v[2:17], v[132:137], 1.0
	v_mov_b32_e32 v27, 0
	v_mov_b32_e32 v29, 0
	v_dot2c_f32_bf16_e32 v27, v2, v78
	v_dot2c_f32_bf16_e32 v29, v3, v79
	v_dot2c_f32_bf16_e32 v27, v4, v80
	v_dot2c_f32_bf16_e32 v29, v5, v81
	v_dot2c_f32_bf16_e32 v27, v6, v74
	v_dot2c_f32_bf16_e32 v29, v7, v75
	v_dot2c_f32_bf16_e32 v27, v8, v76
	v_dot2c_f32_bf16_e32 v29, v9, v77
	v_dot2c_f32_bf16_e32 v27, v10, v70
	v_dot2c_f32_bf16_e32 v29, v11, v71
	v_dot2c_f32_bf16_e32 v27, v12, v72
	v_dot2c_f32_bf16_e32 v29, v13, v73
	v_dot2c_f32_bf16_e32 v100, v31, v67
	v_dot2c_f32_bf16_e32 v27, v14, v66
	v_dot2c_f32_bf16_e32 v29, v15, v67
	v_dot2c_f32_bf16_e32 v100, v33, v69
	v_dot2c_f32_bf16_e32 v27, v16, v68
	v_dot2c_f32_bf16_e32 v29, v17, v69
	s_waitcnt vmcnt(0)
	v_cvt_scalef32_pk32_bf16_fp6 v[2:17], v[138:143], 1.0
	v_mov_b32_e32 v31, 0
	v_mov_b32_e32 v33, 0
	v_dot2c_f32_bf16_e32 v31, v2, v78
	v_dot2c_f32_bf16_e32 v33, v3, v79
	v_dot2c_f32_bf16_e32 v31, v4, v80
	v_dot2c_f32_bf16_e32 v33, v5, v81
	v_dot2c_f32_bf16_e32 v31, v6, v74
	v_dot2c_f32_bf16_e32 v33, v7, v75
	v_dot2c_f32_bf16_e32 v31, v8, v76
	v_dot2c_f32_bf16_e32 v33, v9, v77
	v_dot2c_f32_bf16_e32 v31, v10, v70
	v_dot2c_f32_bf16_e32 v33, v11, v71
	v_dot2c_f32_bf16_e32 v31, v12, v72
	v_dot2c_f32_bf16_e32 v33, v13, v73
	v_dot2c_f32_bf16_e32 v31, v14, v66
	v_dot2c_f32_bf16_e32 v33, v15, v67
	v_pk_add_f32 v[8:9], v[104:105], v[102:103]
	v_pk_add_f32 v[10:11], v[24:25], v[22:23]
	v_dot2c_f32_bf16_e32 v31, v16, v68
	v_dot2c_f32_bf16_e32 v33, v17, v69
	v_cndmask_b32_e64 v7, v8, v10, s[4:5]
	v_pk_add_f32 v[14:15], v[100:101], v[98:99]
	v_pk_add_f32 v[16:17], v[28:29], v[26:27]
	v_dot2c_f32_bf16_e32 v106, v64, v68
	v_dot2c_f32_bf16_e32 v108, v65, v69
	v_pk_add_f32 v[4:5], v[20:21], v[18:19]
	s_nop 1
	v_mov_b32_dpp v12, v7 row_shl:4 row_mask:0xf bank_mask:0x5
	v_mov_b32_dpp v12, v7 row_shr:4 row_mask:0xf bank_mask:0xa
	v_cndmask_b32_e64 v7, v14, v16, s[4:5]
	v_pk_add_f32 v[20:21], v[96:97], v[94:95]
	v_pk_add_f32 v[22:23], v[32:33], v[30:31]
	v_pk_add_f32 v[2:3], v[108:109], v[106:107]
	s_nop 1
	v_mov_b32_dpp v18, v7 row_shl:4 row_mask:0xf bank_mask:0x5
	v_mov_b32_dpp v18, v7 row_shr:4 row_mask:0xf bank_mask:0xa
	v_cndmask_b32_e64 v7, v20, v22, s[4:5]
	v_cndmask_b32_e64 v6, v2, v4, s[4:5]
	s_nop 1
	v_mov_b32_dpp v24, v7 row_shl:4 row_mask:0xf bank_mask:0x5
	v_mov_b32_dpp v24, v7 row_shr:4 row_mask:0xf bank_mask:0xa
	v_cndmask_b32_e64 v7, v3, v5, s[4:5]
	s_nop 1
	v_mov_b32_dpp v190, v6 row_shl:4 row_mask:0xf bank_mask:0x5
	v_mov_b32_dpp v190, v6 row_shr:4 row_mask:0xf bank_mask:0xa
	v_mov_b32_e32 v6, v190
	s_nop 1
	v_mov_b32_dpp v191, v7 row_shl:4 row_mask:0xf bank_mask:0x5
	v_mov_b32_dpp v191, v7 row_shr:4 row_mask:0xf bank_mask:0xa
	v_mov_b32_e32 v7, v191
	v_cndmask_b32_e64 v3, v5, v3, s[4:5]
	v_cndmask_b32_e64 v2, v4, v2, s[4:5]
	v_cndmask_b32_e64 v5, v15, v17, s[4:5]
	s_nop 1
	v_mov_b32_dpp v19, v5 row_shl:4 row_mask:0xf bank_mask:0x5
	v_mov_b32_dpp v19, v5 row_shr:4 row_mask:0xf bank_mask:0xa
	s_waitcnt lgkmcnt(1)
	v_pk_add_f32 v[2:3], v[2:3], v[6:7]
	v_cndmask_b32_e64 v7, v9, v11, s[4:5]
	s_nop 1
	v_mov_b32_dpp v13, v7 row_shl:4 row_mask:0xf bank_mask:0x5
	v_mov_b32_dpp v13, v7 row_shr:4 row_mask:0xf bank_mask:0xa
	v_cndmask_b32_e64 v7, v21, v23, s[4:5]
	s_nop 1
	v_mov_b32_dpp v25, v7 row_shl:4 row_mask:0xf bank_mask:0x5
	v_mov_b32_dpp v25, v7 row_shr:4 row_mask:0xf bank_mask:0xa
	v_cndmask_b32_e64 v9, v11, v9, s[4:5]
	v_cndmask_b32_e64 v8, v10, v8, s[4:5]
	v_cndmask_b32_e64 v11, v23, v21, s[4:5]
	v_cndmask_b32_e64 v10, v22, v20, s[4:5]
	v_cndmask_b32_e64 v5, v17, v15, s[4:5]
	v_cndmask_b32_e64 v4, v16, v14, s[4:5]
	s_waitcnt lgkmcnt(1)
	v_pk_add_f32 v[8:9], v[8:9], v[12:13]
	s_waitcnt lgkmcnt(0)
	v_pk_add_f32 v[10:11], v[10:11], v[24:25]
	v_pk_add_f32 v[4:5], v[4:5], v[18:19]
	v_cndmask_b32_e64 v7, v8, v10, s[6:7]
	v_cndmask_b32_e64 v6, v2, v4, s[6:7]
	s_nop 1
	v_mov_b32_dpp v12, v7 quad_perm:[2,3,0,1] row_mask:0xf bank_mask:0xf
	v_cndmask_b32_e64 v7, v3, v5, s[6:7]
	v_cndmask_b32_e64 v3, v5, v3, s[6:7]
	v_cndmask_b32_e64 v5, v9, v11, s[6:7]
	s_nop 1
	v_mov_b32_dpp v6, v6 quad_perm:[2,3,0,1] row_mask:0xf bank_mask:0xf
	s_nop 1
	v_mov_b32_dpp v7, v7 quad_perm:[2,3,0,1] row_mask:0xf bank_mask:0xf
	s_nop 1
	v_mov_b32_dpp v13, v5 quad_perm:[2,3,0,1] row_mask:0xf bank_mask:0xf
	v_cndmask_b32_e64 v2, v4, v2, s[6:7]
	v_cndmask_b32_e64 v5, v11, v9, s[6:7]
	v_cndmask_b32_e64 v4, v10, v8, s[6:7]
	s_waitcnt lgkmcnt(1)
	v_pk_add_f32 v[2:3], v[2:3], v[6:7]
	s_waitcnt lgkmcnt(0)
	v_pk_add_f32 v[4:5], v[4:5], v[12:13]
	s_nop 0
	v_cndmask_b32_e64 v6, v2, v4, s[8:9]
	v_cndmask_b32_e64 v7, v3, v5, s[8:9]
	s_nop 1
	v_mov_b32_dpp v6, v6 quad_perm:[1,0,3,2] row_mask:0xf bank_mask:0xf
	s_nop 1
	v_mov_b32_dpp v7, v7 quad_perm:[1,0,3,2] row_mask:0xf bank_mask:0xf
	v_cndmask_b32_e64 v3, v5, v3, s[8:9]
	v_cndmask_b32_e64 v2, v4, v2, s[8:9]
	s_waitcnt lgkmcnt(0)
	v_pk_add_f32 v[2:3], v[2:3], v[6:7]
	s_cbranch_vccnz .LBB0_743
	ds_read2st64_b32 v[4:5], v124 offset1:1
	s_waitcnt lgkmcnt(0)
	v_pk_add_f32 v[2:3], v[2:3], v[4:5]
	s_branch .LBB0_743

.LBB0_1495:
	ds_read_b128 v[2:5], v123
	ds_read_b128 v[82:85], v123 offset:128
	v_mov_b32_e32 v94, 0
	v_mov_b32_e32 v96, 0
	v_mov_b32_e32 v98, 0
	s_waitcnt lgkmcnt(0)
	v_and_b32_e32 v6, 0xffff, v2
	v_lshrrev_b32_e32 v2, 16, v2
	v_mad_u32_u24 v18, v6, s25, v110
	v_mad_u32_u24 v2, v2, s25, v110
	global_load_dwordx2 v[10:11], v18, s[20:21] offset:16
	global_load_dwordx4 v[6:9], v18, s[20:21]
	global_load_dwordx2 v[16:17], v2, s[20:21] offset:16
	global_load_dwordx4 v[12:15], v2, s[20:21]
	v_and_b32_e32 v2, 0xffff, v3
	v_mad_u32_u24 v2, v2, s25, v110
	global_load_dwordx2 v[130:131], v2, s[20:21] offset:16
	global_load_dwordx4 v[126:129], v2, s[20:21]
	v_lshrrev_b32_e32 v2, 16, v3
	v_mad_u32_u24 v2, v2, s25, v110
	global_load_dwordx2 v[136:137], v2, s[20:21] offset:16
	global_load_dwordx4 v[132:135], v2, s[20:21]
	v_and_b32_e32 v2, 0xffff, v4
	v_mad_u32_u24 v2, v2, s25, v110
	global_load_dwordx2 v[142:143], v2, s[20:21] offset:16
	global_load_dwordx4 v[138:141], v2, s[20:21]
	v_lshrrev_b32_e32 v3, 16, v4
	v_and_b32_e32 v2, 0xffff, v5
	v_lshrrev_b32_e32 v4, 16, v5
	v_mad_u32_u24 v3, v3, s25, v110
	v_mad_u32_u24 v2, v2, s25, v110
	v_mad_u32_u24 v4, v4, s25, v110
	global_load_dwordx2 v[148:149], v3, s[20:21] offset:16
	global_load_dwordx4 v[144:147], v3, s[20:21]
	global_load_dwordx2 v[154:155], v2, s[20:21] offset:16
	global_load_dwordx4 v[150:153], v2, s[20:21]
	global_load_dwordx2 v[160:161], v4, s[20:21] offset:16
	global_load_dwordx4 v[156:159], v4, s[20:21]
	v_mov_b32_e32 v102, 0
	v_mov_b32_e32 v104, 0
	v_mov_b32_e32 v100, 0
	v_mov_b32_e32 v106, 0
	v_mov_b32_e32 v108, 0
	v_mov_b32_e32 v107, 0
	v_mov_b32_e32 v109, 0
	v_mov_b32_e32 v103, 0
	v_mov_b32_e32 v105, 0
	v_mov_b32_e32 v99, 0
	v_mov_b32_e32 v101, 0
	v_mov_b32_e32 v95, 0
	v_mov_b32_e32 v97, 0
	s_and_b64 vcc, exec, s[10:11]
	s_waitcnt vmcnt(14)
	v_cvt_scalef32_pk32_bf16_fp6 v[50:65], v[6:11], 1.0
	v_dot2c_f32_bf16_e32 v106, v50, v78
	s_waitcnt vmcnt(12)
	v_cvt_scalef32_pk32_bf16_fp6 v[34:49], v[12:17], 1.0
	v_dot2c_f32_bf16_e32 v102, v34, v78
	v_dot2c_f32_bf16_e32 v104, v35, v79
	s_waitcnt vmcnt(10)
	v_cvt_scalef32_pk32_bf16_fp6 v[18:33], v[126:131], 1.0
	v_dot2c_f32_bf16_e32 v98, v18, v78
	v_dot2c_f32_bf16_e32 v98, v20, v80
	s_waitcnt vmcnt(8)
	v_cvt_scalef32_pk32_bf16_fp6 v[2:17], v[132:137], 1.0
	v_dot2c_f32_bf16_e32 v94, v2, v78
	v_dot2c_f32_bf16_e32 v96, v3, v79
	v_dot2c_f32_bf16_e32 v94, v4, v80
	v_dot2c_f32_bf16_e32 v96, v5, v81
	v_dot2c_f32_bf16_e32 v94, v6, v74
	v_dot2c_f32_bf16_e32 v96, v7, v75
	v_dot2c_f32_bf16_e32 v94, v8, v76
	v_dot2c_f32_bf16_e32 v96, v9, v77
	v_dot2c_f32_bf16_e32 v94, v10, v70
	v_dot2c_f32_bf16_e32 v96, v11, v71
	v_dot2c_f32_bf16_e32 v94, v12, v72
	v_dot2c_f32_bf16_e32 v96, v13, v73
	v_dot2c_f32_bf16_e32 v94, v14, v66
	v_dot2c_f32_bf16_e32 v96, v15, v67
	v_dot2c_f32_bf16_e32 v94, v16, v68
	v_dot2c_f32_bf16_e32 v96, v17, v69
	s_waitcnt vmcnt(6)
	v_cvt_scalef32_pk32_bf16_fp6 v[2:17], v[138:143], 1.0
	v_mov_b32_e32 v18, 0
	v_mov_b32_e32 v20, 0
	v_dot2c_f32_bf16_e32 v18, v2, v78
	v_dot2c_f32_bf16_e32 v20, v3, v79
	v_dot2c_f32_bf16_e32 v18, v4, v80
	v_dot2c_f32_bf16_e32 v20, v5, v81
	v_dot2c_f32_bf16_e32 v18, v6, v74
	v_dot2c_f32_bf16_e32 v20, v7, v75
	v_dot2c_f32_bf16_e32 v18, v8, v76
	v_dot2c_f32_bf16_e32 v20, v9, v77
	v_dot2c_f32_bf16_e32 v18, v10, v70
	v_dot2c_f32_bf16_e32 v20, v11, v71
	v_dot2c_f32_bf16_e32 v18, v12, v72
	v_dot2c_f32_bf16_e32 v20, v13, v73
	v_dot2c_f32_bf16_e32 v18, v14, v66
	v_dot2c_f32_bf16_e32 v20, v15, v67
	v_dot2c_f32_bf16_e32 v98, v22, v74
	v_dot2c_f32_bf16_e32 v18, v16, v68
	v_dot2c_f32_bf16_e32 v20, v17, v69
	s_waitcnt vmcnt(4)
	v_cvt_scalef32_pk32_bf16_fp6 v[2:17], v[144:149], 1.0
	v_mov_b32_e32 v22, 0
	v_dot2c_f32_bf16_e32 v22, v2, v78
	v_and_b32_e32 v2, 0xffff, v82
	v_dot2c_f32_bf16_e32 v102, v36, v80
	v_dot2c_f32_bf16_e32 v104, v37, v81
	v_mad_u32_u24 v2, v2, s25, v110
	v_dot2c_f32_bf16_e32 v102, v38, v74
	v_dot2c_f32_bf16_e32 v104, v39, v75
	global_load_dwordx2 v[38:39], v2, s[20:21] offset:16
	global_load_dwordx4 v[34:37], v2, s[20:21]
	v_dot2c_f32_bf16_e32 v98, v24, v76
	v_mov_b32_e32 v24, 0
	v_dot2c_f32_bf16_e32 v100, v19, v79
	v_dot2c_f32_bf16_e32 v102, v40, v76
	v_dot2c_f32_bf16_e32 v104, v41, v77
	v_dot2c_f32_bf16_e32 v24, v3, v79
	v_lshrrev_b32_e32 v19, 16, v82
	v_dot2c_f32_bf16_e32 v102, v42, v70
	v_dot2c_f32_bf16_e32 v104, v43, v71
	v_dot2c_f32_bf16_e32 v22, v4, v80
	v_dot2c_f32_bf16_e32 v24, v5, v81
	v_mad_u32_u24 v19, v19, s25, v110
	v_dot2c_f32_bf16_e32 v102, v44, v72
	v_dot2c_f32_bf16_e32 v104, v45, v73
	v_dot2c_f32_bf16_e32 v22, v6, v74
	v_dot2c_f32_bf16_e32 v24, v7, v75
	global_load_dwordx2 v[44:45], v19, s[20:21] offset:16
	global_load_dwordx4 v[40:43], v19, s[20:21]
	v_dot2c_f32_bf16_e32 v22, v8, v76
	v_dot2c_f32_bf16_e32 v24, v9, v77
	v_dot2c_f32_bf16_e32 v22, v10, v70
	v_dot2c_f32_bf16_e32 v24, v11, v71
	v_dot2c_f32_bf16_e32 v22, v12, v72
	v_dot2c_f32_bf16_e32 v24, v13, v73
	v_dot2c_f32_bf16_e32 v98, v26, v70
	v_dot2c_f32_bf16_e32 v22, v14, v66
	v_dot2c_f32_bf16_e32 v24, v15, v67
	v_dot2c_f32_bf16_e32 v98, v28, v72
	v_dot2c_f32_bf16_e32 v22, v16, v68
	v_dot2c_f32_bf16_e32 v24, v17, v69
	s_waitcnt vmcnt(6)
	v_cvt_scalef32_pk32_bf16_fp6 v[2:17], v[150:155], 1.0
	v_mov_b32_e32 v26, 0
	v_mov_b32_e32 v28, 0
	v_dot2c_f32_bf16_e32 v26, v2, v78
	v_dot2c_f32_bf16_e32 v28, v3, v79
	v_and_b32_e32 v2, 0xffff, v83
	v_dot2c_f32_bf16_e32 v102, v46, v66
	v_dot2c_f32_bf16_e32 v104, v47, v67
	v_dot2c_f32_bf16_e32 v26, v4, v80
	v_dot2c_f32_bf16_e32 v28, v5, v81
	v_mad_u32_u24 v2, v2, s25, v110
	v_dot2c_f32_bf16_e32 v108, v51, v79
	v_dot2c_f32_bf16_e32 v102, v48, v68
	v_dot2c_f32_bf16_e32 v104, v49, v69
	v_dot2c_f32_bf16_e32 v26, v6, v74
	v_dot2c_f32_bf16_e32 v28, v7, v75
	global_load_dwordx2 v[50:51], v2, s[20:21] offset:16
	global_load_dwordx4 v[46:49], v2, s[20:21]
	v_dot2c_f32_bf16_e32 v26, v8, v76
	v_dot2c_f32_bf16_e32 v28, v9, v77
	v_dot2c_f32_bf16_e32 v26, v10, v70
	v_dot2c_f32_bf16_e32 v28, v11, v71
	v_dot2c_f32_bf16_e32 v26, v12, v72
	v_dot2c_f32_bf16_e32 v28, v13, v73
	v_dot2c_f32_bf16_e32 v26, v14, v66
	v_dot2c_f32_bf16_e32 v28, v15, v67
	v_dot2c_f32_bf16_e32 v98, v30, v66
	v_dot2c_f32_bf16_e32 v26, v16, v68
	v_dot2c_f32_bf16_e32 v28, v17, v69
	s_waitcnt vmcnt(6)
	v_cvt_scalef32_pk32_bf16_fp6 v[2:17], v[156:161], 1.0
	v_mov_b32_e32 v30, 0
	v_dot2c_f32_bf16_e32 v106, v52, v80
	v_dot2c_f32_bf16_e32 v108, v53, v81
	v_dot2c_f32_bf16_e32 v30, v2, v78
	v_lshrrev_b32_e32 v2, 16, v83
	v_dot2c_f32_bf16_e32 v106, v54, v74
	v_dot2c_f32_bf16_e32 v108, v55, v75
	v_mad_u32_u24 v2, v2, s25, v110
	v_dot2c_f32_bf16_e32 v106, v56, v76
	v_dot2c_f32_bf16_e32 v108, v57, v77
	global_load_dwordx2 v[56:57], v2, s[20:21] offset:16
	global_load_dwordx4 v[52:55], v2, s[20:21]
	v_dot2c_f32_bf16_e32 v106, v58, v70
	v_dot2c_f32_bf16_e32 v108, v59, v71
	v_and_b32_e32 v2, 0xffff, v84
	v_dot2c_f32_bf16_e32 v106, v60, v72
	v_dot2c_f32_bf16_e32 v108, v61, v73
	v_mad_u32_u24 v2, v2, s25, v110
	v_dot2c_f32_bf16_e32 v106, v62, v66
	v_dot2c_f32_bf16_e32 v108, v63, v67
	global_load_dwordx2 v[62:63], v2, s[20:21] offset:16
	global_load_dwordx4 v[58:61], v2, s[20:21]
	v_lshrrev_b32_e32 v2, 16, v84
	v_mad_u32_u24 v2, v2, s25, v110
	global_load_dwordx2 v[130:131], v2, s[20:21] offset:16
	global_load_dwordx4 v[126:129], v2, s[20:21]
	v_and_b32_e32 v2, 0xffff, v85
	v_mad_u32_u24 v2, v2, s25, v110
	global_load_dwordx2 v[136:137], v2, s[20:21] offset:16
	global_load_dwordx4 v[132:135], v2, s[20:21]
	v_lshrrev_b32_e32 v2, 16, v85
	v_mad_u32_u24 v2, v2, s25, v110
	global_load_dwordx2 v[142:143], v2, s[20:21] offset:16
	global_load_dwordx4 v[138:141], v2, s[20:21]
	v_dot2c_f32_bf16_e32 v98, v32, v68
	v_mov_b32_e32 v32, 0
	v_dot2c_f32_bf16_e32 v32, v3, v79
	v_dot2c_f32_bf16_e32 v30, v4, v80
	v_dot2c_f32_bf16_e32 v32, v5, v81
	v_dot2c_f32_bf16_e32 v30, v6, v74
	v_dot2c_f32_bf16_e32 v32, v7, v75
	v_dot2c_f32_bf16_e32 v30, v8, v76
	v_dot2c_f32_bf16_e32 v32, v9, v77
	v_dot2c_f32_bf16_e32 v30, v10, v70
	v_dot2c_f32_bf16_e32 v32, v11, v71
	v_dot2c_f32_bf16_e32 v30, v12, v72
	v_dot2c_f32_bf16_e32 v32, v13, v73
	v_dot2c_f32_bf16_e32 v30, v14, v66
	v_dot2c_f32_bf16_e32 v32, v15, v67
	v_dot2c_f32_bf16_e32 v30, v16, v68
	v_dot2c_f32_bf16_e32 v32, v17, v69
	s_waitcnt vmcnt(14)
	v_cvt_scalef32_pk32_bf16_fp6 v[2:17], v[34:39], 1.0
	v_dot2c_f32_bf16_e32 v107, v2, v78
	v_dot2c_f32_bf16_e32 v109, v3, v79
	v_dot2c_f32_bf16_e32 v107, v4, v80
	v_dot2c_f32_bf16_e32 v109, v5, v81
	v_dot2c_f32_bf16_e32 v107, v6, v74
	v_dot2c_f32_bf16_e32 v109, v7, v75
	v_dot2c_f32_bf16_e32 v107, v8, v76
	v_dot2c_f32_bf16_e32 v109, v9, v77
	v_dot2c_f32_bf16_e32 v107, v10, v70
	v_dot2c_f32_bf16_e32 v109, v11, v71
	v_dot2c_f32_bf16_e32 v107, v12, v72
	v_dot2c_f32_bf16_e32 v109, v13, v73
	v_dot2c_f32_bf16_e32 v107, v14, v66
	v_dot2c_f32_bf16_e32 v109, v15, v67
	v_dot2c_f32_bf16_e32 v107, v16, v68
	v_dot2c_f32_bf16_e32 v109, v17, v69
	s_waitcnt vmcnt(12)
	v_cvt_scalef32_pk32_bf16_fp6 v[2:17], v[40:45], 1.0
	v_dot2c_f32_bf16_e32 v103, v2, v78
	v_dot2c_f32_bf16_e32 v105, v3, v79
	v_dot2c_f32_bf16_e32 v103, v4, v80
	v_dot2c_f32_bf16_e32 v105, v5, v81
	v_dot2c_f32_bf16_e32 v103, v6, v74
	v_dot2c_f32_bf16_e32 v105, v7, v75
	v_dot2c_f32_bf16_e32 v103, v8, v76
	v_dot2c_f32_bf16_e32 v105, v9, v77
	v_dot2c_f32_bf16_e32 v103, v10, v70
	v_dot2c_f32_bf16_e32 v105, v11, v71
	v_dot2c_f32_bf16_e32 v103, v12, v72
	v_dot2c_f32_bf16_e32 v105, v13, v73
	v_dot2c_f32_bf16_e32 v103, v14, v66
	v_dot2c_f32_bf16_e32 v105, v15, v67
	v_dot2c_f32_bf16_e32 v103, v16, v68
	v_dot2c_f32_bf16_e32 v105, v17, v69
	s_waitcnt vmcnt(10)
	v_cvt_scalef32_pk32_bf16_fp6 v[2:17], v[46:51], 1.0
	v_dot2c_f32_bf16_e32 v99, v2, v78
	v_dot2c_f32_bf16_e32 v101, v3, v79
	v_dot2c_f32_bf16_e32 v99, v4, v80
	v_dot2c_f32_bf16_e32 v101, v5, v81
	v_dot2c_f32_bf16_e32 v99, v6, v74
	v_dot2c_f32_bf16_e32 v101, v7, v75
	v_dot2c_f32_bf16_e32 v99, v8, v76
	v_dot2c_f32_bf16_e32 v101, v9, v77
	v_dot2c_f32_bf16_e32 v99, v10, v70
	v_dot2c_f32_bf16_e32 v101, v11, v71
	v_dot2c_f32_bf16_e32 v99, v12, v72
	v_dot2c_f32_bf16_e32 v101, v13, v73
	v_dot2c_f32_bf16_e32 v99, v14, v66
	v_dot2c_f32_bf16_e32 v101, v15, v67
	v_dot2c_f32_bf16_e32 v99, v16, v68
	v_dot2c_f32_bf16_e32 v101, v17, v69
	s_waitcnt vmcnt(8)
	v_cvt_scalef32_pk32_bf16_fp6 v[2:17], v[52:57], 1.0
	v_dot2c_f32_bf16_e32 v95, v2, v78
	v_dot2c_f32_bf16_e32 v97, v3, v79
	v_dot2c_f32_bf16_e32 v95, v4, v80
	v_dot2c_f32_bf16_e32 v97, v5, v81
	v_dot2c_f32_bf16_e32 v95, v6, v74
	v_dot2c_f32_bf16_e32 v97, v7, v75
	v_dot2c_f32_bf16_e32 v95, v8, v76
	v_dot2c_f32_bf16_e32 v97, v9, v77
	v_dot2c_f32_bf16_e32 v95, v10, v70
	v_dot2c_f32_bf16_e32 v97, v11, v71
	v_dot2c_f32_bf16_e32 v95, v12, v72
	v_dot2c_f32_bf16_e32 v97, v13, v73
	v_dot2c_f32_bf16_e32 v95, v14, v66
	v_dot2c_f32_bf16_e32 v97, v15, v67
	v_dot2c_f32_bf16_e32 v100, v21, v81
	v_dot2c_f32_bf16_e32 v95, v16, v68
	v_dot2c_f32_bf16_e32 v97, v17, v69
	s_waitcnt vmcnt(6)
	v_cvt_scalef32_pk32_bf16_fp6 v[2:17], v[58:63], 1.0
	v_mov_b32_e32 v19, 0
	v_mov_b32_e32 v21, 0
	v_dot2c_f32_bf16_e32 v19, v2, v78
	v_dot2c_f32_bf16_e32 v21, v3, v79
	v_dot2c_f32_bf16_e32 v19, v4, v80
	v_dot2c_f32_bf16_e32 v21, v5, v81
	v_dot2c_f32_bf16_e32 v19, v6, v74
	v_dot2c_f32_bf16_e32 v21, v7, v75
	v_dot2c_f32_bf16_e32 v19, v8, v76
	v_dot2c_f32_bf16_e32 v21, v9, v77
	v_dot2c_f32_bf16_e32 v19, v10, v70
	v_dot2c_f32_bf16_e32 v21, v11, v71
	v_dot2c_f32_bf16_e32 v19, v12, v72
	v_dot2c_f32_bf16_e32 v21, v13, v73
	v_dot2c_f32_bf16_e32 v100, v23, v75
	v_dot2c_f32_bf16_e32 v19, v14, v66
	v_dot2c_f32_bf16_e32 v21, v15, v67
	v_dot2c_f32_bf16_e32 v100, v25, v77
	v_dot2c_f32_bf16_e32 v19, v16, v68
	v_dot2c_f32_bf16_e32 v21, v17, v69
	s_waitcnt vmcnt(4)
	v_cvt_scalef32_pk32_bf16_fp6 v[2:17], v[126:131], 1.0
	v_mov_b32_e32 v23, 0
	v_mov_b32_e32 v25, 0
	v_dot2c_f32_bf16_e32 v23, v2, v78
	v_dot2c_f32_bf16_e32 v25, v3, v79
	v_dot2c_f32_bf16_e32 v23, v4, v80
	v_dot2c_f32_bf16_e32 v25, v5, v81
	v_dot2c_f32_bf16_e32 v23, v6, v74
	v_dot2c_f32_bf16_e32 v25, v7, v75
	v_dot2c_f32_bf16_e32 v23, v8, v76
	v_dot2c_f32_bf16_e32 v25, v9, v77
	v_dot2c_f32_bf16_e32 v23, v10, v70
	v_dot2c_f32_bf16_e32 v25, v11, v71
	v_dot2c_f32_bf16_e32 v23, v12, v72
	v_dot2c_f32_bf16_e32 v25, v13, v73
	v_dot2c_f32_bf16_e32 v100, v27, v71
	v_dot2c_f32_bf16_e32 v23, v14, v66
	v_dot2c_f32_bf16_e32 v25, v15, v67
	v_dot2c_f32_bf16_e32 v100, v29, v73
	v_dot2c_f32_bf16_e32 v23, v16, v68
	v_dot2c_f32_bf16_e32 v25, v17, v69
	s_waitcnt vmcnt(2)
	v_cvt_scalef32_pk32_bf16_fp6 v[2:17], v[132:137], 1.0
	v_mov_b32_e32 v27, 0
	v_mov_b32_e32 v29, 0
	v_dot2c_f32_bf16_e32 v27, v2, v78
	v_dot2c_f32_bf16_e32 v29, v3, v79
	v_dot2c_f32_bf16_e32 v27, v4, v80
	v_dot2c_f32_bf16_e32 v29, v5, v81
	v_dot2c_f32_bf16_e32 v27, v6, v74
	v_dot2c_f32_bf16_e32 v29, v7, v75
	v_dot2c_f32_bf16_e32 v27, v8, v76
	v_dot2c_f32_bf16_e32 v29, v9, v77
	v_dot2c_f32_bf16_e32 v27, v10, v70
	v_dot2c_f32_bf16_e32 v29, v11, v71
	v_dot2c_f32_bf16_e32 v27, v12, v72
	v_dot2c_f32_bf16_e32 v29, v13, v73
	v_dot2c_f32_bf16_e32 v100, v31, v67
	v_dot2c_f32_bf16_e32 v27, v14, v66
	v_dot2c_f32_bf16_e32 v29, v15, v67
	v_dot2c_f32_bf16_e32 v100, v33, v69
	v_dot2c_f32_bf16_e32 v27, v16, v68
	v_dot2c_f32_bf16_e32 v29, v17, v69
	s_waitcnt vmcnt(0)
	v_cvt_scalef32_pk32_bf16_fp6 v[2:17], v[138:143], 1.0
	v_mov_b32_e32 v31, 0
	v_mov_b32_e32 v33, 0
	v_dot2c_f32_bf16_e32 v31, v2, v78
	v_dot2c_f32_bf16_e32 v33, v3, v79
	v_dot2c_f32_bf16_e32 v31, v4, v80
	v_dot2c_f32_bf16_e32 v33, v5, v81
	v_dot2c_f32_bf16_e32 v31, v6, v74
	v_dot2c_f32_bf16_e32 v33, v7, v75
	v_dot2c_f32_bf16_e32 v31, v8, v76
	v_dot2c_f32_bf16_e32 v33, v9, v77
	v_dot2c_f32_bf16_e32 v31, v10, v70
	v_dot2c_f32_bf16_e32 v33, v11, v71
	v_dot2c_f32_bf16_e32 v31, v12, v72
	v_dot2c_f32_bf16_e32 v33, v13, v73
	v_dot2c_f32_bf16_e32 v31, v14, v66
	v_dot2c_f32_bf16_e32 v33, v15, v67
	v_pk_add_f32 v[8:9], v[104:105], v[102:103]
	v_pk_add_f32 v[10:11], v[24:25], v[22:23]
	v_dot2c_f32_bf16_e32 v31, v16, v68
	v_dot2c_f32_bf16_e32 v33, v17, v69
	v_cndmask_b32_e64 v7, v8, v10, s[2:3]
	v_pk_add_f32 v[14:15], v[100:101], v[98:99]
	v_pk_add_f32 v[16:17], v[28:29], v[26:27]
	v_dot2c_f32_bf16_e32 v106, v64, v68
	v_dot2c_f32_bf16_e32 v108, v65, v69
	v_pk_add_f32 v[4:5], v[20:21], v[18:19]
	s_nop 1
	v_mov_b32_dpp v12, v7 row_shl:4 row_mask:0xf bank_mask:0x5
	v_mov_b32_dpp v12, v7 row_shr:4 row_mask:0xf bank_mask:0xa
	v_cndmask_b32_e64 v7, v14, v16, s[2:3]
	v_pk_add_f32 v[20:21], v[96:97], v[94:95]
	v_pk_add_f32 v[22:23], v[32:33], v[30:31]
	v_pk_add_f32 v[2:3], v[108:109], v[106:107]
	s_nop 1
	v_mov_b32_dpp v18, v7 row_shl:4 row_mask:0xf bank_mask:0x5
	v_mov_b32_dpp v18, v7 row_shr:4 row_mask:0xf bank_mask:0xa
	v_cndmask_b32_e64 v7, v20, v22, s[2:3]
	v_cndmask_b32_e64 v6, v2, v4, s[2:3]
	s_nop 1
	v_mov_b32_dpp v24, v7 row_shl:4 row_mask:0xf bank_mask:0x5
	v_mov_b32_dpp v24, v7 row_shr:4 row_mask:0xf bank_mask:0xa
	v_cndmask_b32_e64 v7, v3, v5, s[2:3]
	s_nop 1
	v_mov_b32_dpp v190, v6 row_shl:4 row_mask:0xf bank_mask:0x5
	v_mov_b32_dpp v190, v6 row_shr:4 row_mask:0xf bank_mask:0xa
	v_mov_b32_e32 v6, v190
	s_nop 1
	v_mov_b32_dpp v191, v7 row_shl:4 row_mask:0xf bank_mask:0x5
	v_mov_b32_dpp v191, v7 row_shr:4 row_mask:0xf bank_mask:0xa
	v_mov_b32_e32 v7, v191
	v_cndmask_b32_e64 v3, v5, v3, s[2:3]
	v_cndmask_b32_e64 v2, v4, v2, s[2:3]
	v_cndmask_b32_e64 v5, v15, v17, s[2:3]
	s_nop 1
	v_mov_b32_dpp v19, v5 row_shl:4 row_mask:0xf bank_mask:0x5
	v_mov_b32_dpp v19, v5 row_shr:4 row_mask:0xf bank_mask:0xa
	s_waitcnt lgkmcnt(1)
	v_pk_add_f32 v[2:3], v[2:3], v[6:7]
	v_cndmask_b32_e64 v7, v9, v11, s[2:3]
	s_nop 1
	v_mov_b32_dpp v13, v7 row_shl:4 row_mask:0xf bank_mask:0x5
	v_mov_b32_dpp v13, v7 row_shr:4 row_mask:0xf bank_mask:0xa
	v_cndmask_b32_e64 v7, v21, v23, s[2:3]
	s_nop 1
	v_mov_b32_dpp v25, v7 row_shl:4 row_mask:0xf bank_mask:0x5
	v_mov_b32_dpp v25, v7 row_shr:4 row_mask:0xf bank_mask:0xa
	v_cndmask_b32_e64 v9, v11, v9, s[2:3]
	v_cndmask_b32_e64 v8, v10, v8, s[2:3]
	v_cndmask_b32_e64 v11, v23, v21, s[2:3]
	v_cndmask_b32_e64 v10, v22, v20, s[2:3]
	v_cndmask_b32_e64 v5, v17, v15, s[2:3]
	v_cndmask_b32_e64 v4, v16, v14, s[2:3]
	s_waitcnt lgkmcnt(1)
	v_pk_add_f32 v[8:9], v[8:9], v[12:13]
	s_waitcnt lgkmcnt(0)
	v_pk_add_f32 v[10:11], v[10:11], v[24:25]
	v_pk_add_f32 v[4:5], v[4:5], v[18:19]
	v_cndmask_b32_e64 v7, v8, v10, s[4:5]
	v_cndmask_b32_e64 v6, v2, v4, s[4:5]
	s_nop 1
	v_mov_b32_dpp v12, v7 quad_perm:[2,3,0,1] row_mask:0xf bank_mask:0xf
	v_cndmask_b32_e64 v7, v3, v5, s[4:5]
	v_cndmask_b32_e64 v3, v5, v3, s[4:5]
	v_cndmask_b32_e64 v5, v9, v11, s[4:5]
	s_nop 1
	v_mov_b32_dpp v6, v6 quad_perm:[2,3,0,1] row_mask:0xf bank_mask:0xf
	s_nop 1
	v_mov_b32_dpp v7, v7 quad_perm:[2,3,0,1] row_mask:0xf bank_mask:0xf
	s_nop 1
	v_mov_b32_dpp v13, v5 quad_perm:[2,3,0,1] row_mask:0xf bank_mask:0xf
	v_cndmask_b32_e64 v2, v4, v2, s[4:5]
	v_cndmask_b32_e64 v5, v11, v9, s[4:5]
	v_cndmask_b32_e64 v4, v10, v8, s[4:5]
	s_waitcnt lgkmcnt(1)
	v_pk_add_f32 v[2:3], v[2:3], v[6:7]
	s_waitcnt lgkmcnt(0)
	v_pk_add_f32 v[4:5], v[4:5], v[12:13]
	s_nop 0
	v_cndmask_b32_e64 v6, v2, v4, s[6:7]
	v_cndmask_b32_e64 v7, v3, v5, s[6:7]
	s_nop 1
	v_mov_b32_dpp v6, v6 quad_perm:[1,0,3,2] row_mask:0xf bank_mask:0xf
	s_nop 1
	v_mov_b32_dpp v7, v7 quad_perm:[1,0,3,2] row_mask:0xf bank_mask:0xf
	v_cndmask_b32_e64 v3, v5, v3, s[6:7]
	v_cndmask_b32_e64 v2, v4, v2, s[6:7]
	s_waitcnt lgkmcnt(0)
	v_pk_add_f32 v[2:3], v[2:3], v[6:7]
	s_cbranch_vccnz .LBB0_1492
	ds_read2st64_b32 v[4:5], v124 offset1:1
	s_waitcnt lgkmcnt(0)
	v_pk_add_f32 v[2:3], v[2:3], v[4:5]
	s_branch .LBB0_1492
